# MoE up epilogue: silu(gate)*up mul/add steps as packed f32 (same operations and order)
# speedup vs baseline: 1.0109x; 1.0009x over previous
.LBB0_1419:
	ds_read_b128 v[10:13], v130
	ds_read_b128 v[14:17], v130 offset:1024
	ds_read_b128 v[160:163], v130 offset:2048
	ds_read_b128 v[164:167], v130 offset:3072
	s_add_u32 s60, s18, 0xfffe0080
	s_addc_u32 s61, s19, -1
	s_cmp_eq_u32 s75, 4
	s_cselect_b32 s63, s15, s61
	s_cselect_b32 s62, s14, s60
	s_cselect_b32 s61, s17, s74
	s_cselect_b32 s60, s16, s73
	s_mov_b32 m0, s13
	v_lshl_add_u64 v[2:3], s[18:19], 0, v[156:157]
	ds_read_b128 v[178:181], v170
	ds_read_b128 v[182:185], v170 offset:1024
	ds_read_b128 v[186:189], v170 offset:2048
	ds_read_b128 v[190:193], v170 offset:3072
	ds_read_b128 v[194:197], v170 offset:4096
	ds_read_b128 v[198:201], v170 offset:5120
	ds_read_b128 v[218:221], v170 offset:6144
	ds_read_b128 v[222:225], v170 offset:7168
	global_load_lds_dwordx4 v[2:3], off
	v_lshl_add_u64 v[2:3], s[18:19], 0, v[158:159]
	s_mov_b32 m0, s64
	s_nop 0
	global_load_lds_dwordx4 v[2:3], off
	s_waitcnt lgkmcnt(8)
	s_waitcnt vmcnt(10)
	s_barrier
	s_waitcnt lgkmcnt(0)
	s_setprio 1
	s_waitcnt lgkmcnt(0)
	v_mfma_scale_f32_16x16x128_f8f6f4 v[140:143], v[10:17], v[178:185], v[140:143], v205, v205 op_sel_hi:[0,0,0]
	v_mfma_scale_f32_16x16x128_f8f6f4 v[132:135], v[160:167], v[178:185], v[132:135], v205, v205 op_sel_hi:[0,0,0]
	v_mfma_scale_f32_16x16x128_f8f6f4 v[122:125], v[10:17], v[186:193], v[122:125], v205, v205 op_sel_hi:[0,0,0]
	v_mfma_scale_f32_16x16x128_f8f6f4 v[114:117], v[160:167], v[186:193], v[114:117], v205, v205 op_sel_hi:[0,0,0]
	v_mfma_scale_f32_16x16x128_f8f6f4 v[106:109], v[10:17], v[194:201], v[106:109], v205, v205 op_sel_hi:[0,0,0]
	v_mfma_scale_f32_16x16x128_f8f6f4 v[98:101], v[160:167], v[194:201], v[98:101], v205, v205 op_sel_hi:[0,0,0]
	v_mfma_scale_f32_16x16x128_f8f6f4 v[90:93], v[10:17], v[218:225], v[90:93], v205, v205 op_sel_hi:[0,0,0]
	v_mfma_scale_f32_16x16x128_f8f6f4 v[78:81], v[160:167], v[218:225], v[78:81], v205, v205 op_sel_hi:[0,0,0]
	s_setprio 0
	s_barrier
	s_mov_b32 m0, s65
	v_lshl_add_u64 v[6:7], s[60:61], 0, v[154:155]
	ds_read_b128 v[226:229], v171
	ds_read_b128 v[230:233], v171 offset:1024
	ds_read_b128 v[234:237], v171 offset:2048
	ds_read_b128 v[238:241], v171 offset:3072
	global_load_lds_dwordx4 v[6:7], off
	v_lshl_add_u64 v[8:9], s[60:61], 0, v[150:151]
	s_mov_b32 m0, s66
	s_nop 0
	global_load_lds_dwordx4 v[8:9], off
	s_waitcnt vmcnt(10)
	s_barrier
	s_waitcnt lgkmcnt(0)
	s_setprio 1
	s_waitcnt lgkmcnt(0)
	v_mfma_scale_f32_16x16x128_f8f6f4 v[144:147], v[226:233], v[178:185], v[144:147], v205, v205 op_sel_hi:[0,0,0]
	v_mfma_scale_f32_16x16x128_f8f6f4 v[136:139], v[234:241], v[178:185], v[136:139], v205, v205 op_sel_hi:[0,0,0]
	v_mfma_scale_f32_16x16x128_f8f6f4 v[126:129], v[226:233], v[186:193], v[126:129], v205, v205 op_sel_hi:[0,0,0]
	v_mfma_scale_f32_16x16x128_f8f6f4 v[118:121], v[234:241], v[186:193], v[118:121], v205, v205 op_sel_hi:[0,0,0]
	v_mfma_scale_f32_16x16x128_f8f6f4 v[110:113], v[226:233], v[194:201], v[110:113], v205, v205 op_sel_hi:[0,0,0]
	v_mfma_scale_f32_16x16x128_f8f6f4 v[102:105], v[234:241], v[194:201], v[102:105], v205, v205 op_sel_hi:[0,0,0]
	v_mfma_scale_f32_16x16x128_f8f6f4 v[94:97], v[226:233], v[218:225], v[94:97], v205, v205 op_sel_hi:[0,0,0]
	v_mfma_scale_f32_16x16x128_f8f6f4 v[86:89], v[234:241], v[218:225], v[86:89], v205, v205 op_sel_hi:[0,0,0]
	s_setprio 0
	s_mov_b32 m0, s43
	v_lshl_add_u64 v[2:3], s[62:63], 0, v[152:153]
	s_barrier
	ds_read_b128 v[178:181], v170 offset:16384
	ds_read_b128 v[182:185], v170 offset:17408
	ds_read_b128 v[186:189], v170 offset:18432
	ds_read_b128 v[190:193], v170 offset:19456
	ds_read_b128 v[194:197], v170 offset:20480
	ds_read_b128 v[198:201], v170 offset:21504
	ds_read_b128 v[218:221], v170 offset:22528
	ds_read_b128 v[222:225], v170 offset:23552
	global_load_lds_dwordx4 v[2:3], off
	v_lshl_add_u64 v[4:5], s[62:63], 0, v[148:149]
	s_mov_b32 m0, s44
	s_nop 0
	global_load_lds_dwordx4 v[4:5], off
	s_barrier
	s_waitcnt lgkmcnt(0)
	s_setprio 1
	s_waitcnt lgkmcnt(0)
	v_mfma_scale_f32_16x16x128_f8f6f4 v[74:77], v[10:17], v[178:185], v[74:77], v205, v205 op_sel_hi:[0,0,0]
	v_mfma_scale_f32_16x16x128_f8f6f4 v[66:69], v[160:167], v[178:185], v[66:69], v205, v205 op_sel_hi:[0,0,0]
	v_mfma_scale_f32_16x16x128_f8f6f4 v[58:61], v[10:17], v[186:193], v[58:61], v205, v205 op_sel_hi:[0,0,0]
	v_mfma_scale_f32_16x16x128_f8f6f4 v[50:53], v[160:167], v[186:193], v[50:53], v205, v205 op_sel_hi:[0,0,0]
	v_mfma_scale_f32_16x16x128_f8f6f4 v[42:45], v[10:17], v[194:201], v[42:45], v205, v205 op_sel_hi:[0,0,0]
	v_mfma_scale_f32_16x16x128_f8f6f4 v[34:37], v[160:167], v[194:201], v[34:37], v205, v205 op_sel_hi:[0,0,0]
	v_mfma_scale_f32_16x16x128_f8f6f4 v[26:29], v[10:17], v[218:225], v[26:29], v205, v205 op_sel_hi:[0,0,0]
	v_mfma_scale_f32_16x16x128_f8f6f4 v[18:21], v[160:167], v[218:225], v[18:21], v205, v205 op_sel_hi:[0,0,0]
	s_setprio 0
	s_barrier
	s_add_u32 s76, s60, 0x2000
	s_addc_u32 s77, s61, 0
	s_mov_b32 m0, s67
	v_lshl_add_u64 v[10:11], s[76:77], 0, v[154:155]
	global_load_lds_dwordx4 v[10:11], off
	v_lshl_add_u64 v[10:11], s[76:77], 0, v[150:151]
	s_mov_b32 m0, s68
	s_nop 0
	global_load_lds_dwordx4 v[10:11], off
	s_waitcnt vmcnt(10)
	s_barrier
	s_setprio 1
	v_mfma_scale_f32_16x16x128_f8f6f4 v[82:85], v[226:233], v[178:185], v[82:85], v205, v205 op_sel_hi:[0,0,0]
	v_mfma_scale_f32_16x16x128_f8f6f4 v[70:73], v[234:241], v[178:185], v[70:73], v205, v205 op_sel_hi:[0,0,0]
	v_mfma_scale_f32_16x16x128_f8f6f4 v[62:65], v[226:233], v[186:193], v[62:65], v205, v205 op_sel_hi:[0,0,0]
	v_mfma_scale_f32_16x16x128_f8f6f4 v[54:57], v[234:241], v[186:193], v[54:57], v205, v205 op_sel_hi:[0,0,0]
	v_mfma_scale_f32_16x16x128_f8f6f4 v[46:49], v[226:233], v[194:201], v[46:49], v205, v205 op_sel_hi:[0,0,0]
	v_mfma_scale_f32_16x16x128_f8f6f4 v[38:41], v[234:241], v[194:201], v[38:41], v205, v205 op_sel_hi:[0,0,0]
	v_mfma_scale_f32_16x16x128_f8f6f4 v[30:33], v[226:233], v[218:225], v[30:33], v205, v205 op_sel_hi:[0,0,0]
	v_mfma_scale_f32_16x16x128_f8f6f4 v[22:25], v[234:241], v[218:225], v[22:25], v205, v205 op_sel_hi:[0,0,0]
	s_setprio 0
	s_barrier
	ds_read_b128 v[10:13], v172
	ds_read_b128 v[14:17], v172 offset:1024
	ds_read_b128 v[160:163], v172 offset:2048
	ds_read_b128 v[164:167], v172 offset:3072
	s_add_u32 s62, s62, 0x20000
	s_addc_u32 s63, s63, 0
	s_mov_b32 m0, s45
	v_lshl_add_u64 v[174:175], s[62:63], 0, v[152:153]
	ds_read_b128 v[178:181], v170 offset:32768
	ds_read_b128 v[182:185], v170 offset:33792
	ds_read_b128 v[186:189], v170 offset:34816
	ds_read_b128 v[190:193], v170 offset:35840
	ds_read_b128 v[194:197], v170 offset:36864
	ds_read_b128 v[198:201], v170 offset:37888
	ds_read_b128 v[218:221], v170 offset:38912
	ds_read_b128 v[222:225], v170 offset:39936
	global_load_lds_dwordx4 v[174:175], off
	v_lshl_add_u64 v[174:175], s[62:63], 0, v[148:149]
	s_mov_b32 m0, s46
	s_nop 0
	global_load_lds_dwordx4 v[174:175], off
	s_waitcnt lgkmcnt(8)
	s_waitcnt vmcnt(10)
	s_barrier
	s_waitcnt lgkmcnt(0)
	s_setprio 1
	s_waitcnt lgkmcnt(0)
	v_mfma_scale_f32_16x16x128_f8f6f4 v[140:143], v[10:17], v[178:185], v[140:143], v205, v205 op_sel_hi:[0,0,0]
	v_mfma_scale_f32_16x16x128_f8f6f4 v[132:135], v[160:167], v[178:185], v[132:135], v205, v205 op_sel_hi:[0,0,0]
	v_mfma_scale_f32_16x16x128_f8f6f4 v[122:125], v[10:17], v[186:193], v[122:125], v205, v205 op_sel_hi:[0,0,0]
	v_mfma_scale_f32_16x16x128_f8f6f4 v[114:117], v[160:167], v[186:193], v[114:117], v205, v205 op_sel_hi:[0,0,0]
	v_mfma_scale_f32_16x16x128_f8f6f4 v[106:109], v[10:17], v[194:201], v[106:109], v205, v205 op_sel_hi:[0,0,0]
	v_mfma_scale_f32_16x16x128_f8f6f4 v[98:101], v[160:167], v[194:201], v[98:101], v205, v205 op_sel_hi:[0,0,0]
	v_mfma_scale_f32_16x16x128_f8f6f4 v[90:93], v[10:17], v[218:225], v[90:93], v205, v205 op_sel_hi:[0,0,0]
	v_mfma_scale_f32_16x16x128_f8f6f4 v[78:81], v[160:167], v[218:225], v[78:81], v205, v205 op_sel_hi:[0,0,0]
	s_setprio 0
	s_barrier
	s_mov_b32 m0, s69
	v_lshl_add_u64 v[6:7], v[6:7], 0, s[30:31]
	ds_read_b128 v[226:229], v173
	ds_read_b128 v[230:233], v173 offset:1024
	ds_read_b128 v[234:237], v173 offset:2048
	ds_read_b128 v[238:241], v173 offset:3072
	global_load_lds_dwordx4 v[6:7], off
	v_lshl_add_u64 v[6:7], v[8:9], 0, s[30:31]
	s_mov_b32 m0, s70
	s_nop 0
	global_load_lds_dwordx4 v[6:7], off
	s_waitcnt vmcnt(10)
	s_barrier
	s_waitcnt lgkmcnt(0)
	s_setprio 1
	s_waitcnt lgkmcnt(0)
	v_mfma_scale_f32_16x16x128_f8f6f4 v[144:147], v[226:233], v[178:185], v[144:147], v205, v205 op_sel_hi:[0,0,0]
	v_mfma_scale_f32_16x16x128_f8f6f4 v[136:139], v[234:241], v[178:185], v[136:139], v205, v205 op_sel_hi:[0,0,0]
	v_mfma_scale_f32_16x16x128_f8f6f4 v[126:129], v[226:233], v[186:193], v[126:129], v205, v205 op_sel_hi:[0,0,0]
	v_mfma_scale_f32_16x16x128_f8f6f4 v[118:121], v[234:241], v[186:193], v[118:121], v205, v205 op_sel_hi:[0,0,0]
	v_mfma_scale_f32_16x16x128_f8f6f4 v[110:113], v[226:233], v[194:201], v[110:113], v205, v205 op_sel_hi:[0,0,0]
	v_mfma_scale_f32_16x16x128_f8f6f4 v[102:105], v[234:241], v[194:201], v[102:105], v205, v205 op_sel_hi:[0,0,0]
	v_mfma_scale_f32_16x16x128_f8f6f4 v[94:97], v[226:233], v[218:225], v[94:97], v205, v205 op_sel_hi:[0,0,0]
	v_mfma_scale_f32_16x16x128_f8f6f4 v[86:89], v[234:241], v[218:225], v[86:89], v205, v205 op_sel_hi:[0,0,0]
	s_setprio 0
	s_mov_b32 m0, s51
	v_lshl_add_u64 v[2:3], v[2:3], 0, s[30:31]
	s_barrier
	ds_read_b128 v[178:181], v170 offset:49152
	ds_read_b128 v[182:185], v170 offset:50176
	ds_read_b128 v[186:189], v170 offset:51200
	ds_read_b128 v[190:193], v170 offset:52224
	ds_read_b128 v[194:197], v170 offset:53248
	ds_read_b128 v[198:201], v170 offset:54272
	ds_read_b128 v[218:221], v170 offset:55296
	ds_read_b128 v[222:225], v170 offset:56320
	global_load_lds_dwordx4 v[2:3], off
	v_lshl_add_u64 v[2:3], v[4:5], 0, s[30:31]
	s_mov_b32 m0, s53
	s_nop 0
	global_load_lds_dwordx4 v[2:3], off
	s_barrier
	s_waitcnt lgkmcnt(0)
	s_setprio 1
	s_waitcnt lgkmcnt(0)
	v_mfma_scale_f32_16x16x128_f8f6f4 v[74:77], v[10:17], v[178:185], v[74:77], v205, v205 op_sel_hi:[0,0,0]
	v_mfma_scale_f32_16x16x128_f8f6f4 v[66:69], v[160:167], v[178:185], v[66:69], v205, v205 op_sel_hi:[0,0,0]
	v_mfma_scale_f32_16x16x128_f8f6f4 v[58:61], v[10:17], v[186:193], v[58:61], v205, v205 op_sel_hi:[0,0,0]
	v_mfma_scale_f32_16x16x128_f8f6f4 v[50:53], v[160:167], v[186:193], v[50:53], v205, v205 op_sel_hi:[0,0,0]
	v_mfma_scale_f32_16x16x128_f8f6f4 v[42:45], v[10:17], v[194:201], v[42:45], v205, v205 op_sel_hi:[0,0,0]
	v_mfma_scale_f32_16x16x128_f8f6f4 v[34:37], v[160:167], v[194:201], v[34:37], v205, v205 op_sel_hi:[0,0,0]
	v_mfma_scale_f32_16x16x128_f8f6f4 v[26:29], v[10:17], v[218:225], v[26:29], v205, v205 op_sel_hi:[0,0,0]
	v_mfma_scale_f32_16x16x128_f8f6f4 v[18:21], v[160:167], v[218:225], v[18:21], v205, v205 op_sel_hi:[0,0,0]
	s_setprio 0
	s_barrier
	s_add_u32 s60, s60, 0x2080
	s_addc_u32 s61, s61, 0
	s_mov_b32 m0, s71
	v_lshl_add_u64 v[2:3], s[60:61], 0, v[154:155]
	global_load_lds_dwordx4 v[2:3], off
	v_lshl_add_u64 v[2:3], s[60:61], 0, v[150:151]
	s_mov_b32 m0, s72
	s_nop 0
	global_load_lds_dwordx4 v[2:3], off
	s_waitcnt vmcnt(10)
	s_barrier
	s_setprio 1
	v_mfma_scale_f32_16x16x128_f8f6f4 v[82:85], v[226:233], v[178:185], v[82:85], v205, v205 op_sel_hi:[0,0,0]
	v_mfma_scale_f32_16x16x128_f8f6f4 v[70:73], v[234:241], v[178:185], v[70:73], v205, v205 op_sel_hi:[0,0,0]
	v_mfma_scale_f32_16x16x128_f8f6f4 v[62:65], v[226:233], v[186:193], v[62:65], v205, v205 op_sel_hi:[0,0,0]
	v_mfma_scale_f32_16x16x128_f8f6f4 v[54:57], v[234:241], v[186:193], v[54:57], v205, v205 op_sel_hi:[0,0,0]
	v_mfma_scale_f32_16x16x128_f8f6f4 v[46:49], v[226:233], v[194:201], v[46:49], v205, v205 op_sel_hi:[0,0,0]
	v_mfma_scale_f32_16x16x128_f8f6f4 v[38:41], v[234:241], v[194:201], v[38:41], v205, v205 op_sel_hi:[0,0,0]
	v_mfma_scale_f32_16x16x128_f8f6f4 v[30:33], v[226:233], v[218:225], v[30:33], v205, v205 op_sel_hi:[0,0,0]
	v_mfma_scale_f32_16x16x128_f8f6f4 v[22:25], v[234:241], v[218:225], v[22:25], v205, v205 op_sel_hi:[0,0,0]
	s_setprio 0
	s_add_i32 s75, s75, 2
	s_add_u32 s18, s18, 0x100
	s_addc_u32 s19, s19, 0
	s_add_u32 s73, s73, 0x100
	s_addc_u32 s74, s74, 0
	s_cmp_gt_u32 s75, 5
	s_barrier
	s_cbranch_scc0 .LBB0_1419
	v_mov_b32_e32 v234, 0xbcb8aa3b
	v_mov_b32_e32 v235, 0xbcb8aa3b
	v_mov_b32_e32 v236, 1.0
	v_mov_b32_e32 v237, 1.0
	v_mov_b32_e32 v238, 0x3b000000
	v_mov_b32_e32 v239, 0x3b000000
	v_pk_mul_f32 v[218:219], v[140:141], v[234:235]
	v_pk_mul_f32 v[220:221], v[142:143], v[234:235]
	v_pk_mul_f32 v[226:227], v[132:133], v[234:235]
	v_pk_mul_f32 v[228:229], v[134:135], v[234:235]
	v_exp_f32_e32 v218, v218
	v_exp_f32_e32 v219, v219
	v_exp_f32_e32 v220, v220
	v_exp_f32_e32 v221, v221
	v_exp_f32_e32 v226, v226
	v_exp_f32_e32 v227, v227
	v_exp_f32_e32 v228, v228
	v_exp_f32_e32 v229, v229
	v_pk_mul_f32 v[222:223], v[140:141], v[144:145]
	v_pk_mul_f32 v[224:225], v[142:143], v[146:147]
	v_pk_mul_f32 v[230:231], v[132:133], v[136:137]
	v_pk_mul_f32 v[232:233], v[134:135], v[138:139]
	v_pk_add_f32 v[218:219], v[236:237], v[218:219]
	v_pk_add_f32 v[220:221], v[236:237], v[220:221]
	v_pk_add_f32 v[226:227], v[236:237], v[226:227]
	v_pk_add_f32 v[228:229], v[236:237], v[228:229]
	v_rcp_f32_e32 v218, v218
	v_rcp_f32_e32 v219, v219
	v_rcp_f32_e32 v220, v220
	v_rcp_f32_e32 v221, v221
	v_rcp_f32_e32 v226, v226
	v_rcp_f32_e32 v227, v227
	v_rcp_f32_e32 v228, v228
	v_rcp_f32_e32 v229, v229
	v_pk_mul_f32 v[222:223], v[238:239], v[222:223]
	v_pk_mul_f32 v[224:225], v[238:239], v[224:225]
	v_pk_mul_f32 v[230:231], v[238:239], v[230:231]
	v_pk_mul_f32 v[232:233], v[238:239], v[232:233]
	v_pk_mul_f32 v[222:223], v[218:219], v[222:223]
	v_pk_mul_f32 v[224:225], v[220:221], v[224:225]
	v_pk_mul_f32 v[230:231], v[226:227], v[230:231]
	v_pk_mul_f32 v[232:233], v[228:229], v[232:233]
	v_med3_f32 v222, v222, s26, v209
	v_med3_f32 v223, v223, s26, v209
	v_med3_f32 v224, v224, s26, v209
	v_med3_f32 v225, v225, s26, v209
	v_med3_f32 v230, v230, s26, v209
	v_med3_f32 v231, v231, s26, v209
	v_med3_f32 v232, v232, s26, v209
	v_med3_f32 v233, v233, s26, v209
	v_cvt_pk_fp8_f32 v4, v222, v223
	v_cvt_pk_fp8_f32 v4, v224, v225 op_sel:[0,0,1]
	v_cvt_pk_fp8_f32 v5, v230, v231
	v_cvt_pk_fp8_f32 v5, v232, v233 op_sel:[0,0,1]
	s_ashr_i32 s13, s12, 31
	s_lshl_b64 s[12:13], s[12:13], 11
	s_add_u32 s12, s47, s12
	s_addc_u32 s13, s50, s13
	s_ashr_i32 s14, s59, 31
	s_add_u32 s12, s12, s59
	s_addc_u32 s13, s13, s14
	v_mov_b32_e32 v130, v169
	s_nop 15
	s_nop 15
	global_store_dwordx2 v130, v[4:5], s[12:13]
	v_pk_mul_f32 v[218:219], v[122:123], v[234:235]
	v_pk_mul_f32 v[220:221], v[124:125], v[234:235]
	v_pk_mul_f32 v[226:227], v[114:115], v[234:235]
	v_pk_mul_f32 v[228:229], v[116:117], v[234:235]
	v_exp_f32_e32 v218, v218
	v_exp_f32_e32 v219, v219
	v_exp_f32_e32 v220, v220
	v_exp_f32_e32 v221, v221
	v_exp_f32_e32 v226, v226
	v_exp_f32_e32 v227, v227
	v_exp_f32_e32 v228, v228
	v_exp_f32_e32 v229, v229
	v_pk_mul_f32 v[222:223], v[122:123], v[126:127]
	v_pk_mul_f32 v[224:225], v[124:125], v[128:129]
	v_pk_mul_f32 v[230:231], v[114:115], v[118:119]
	v_pk_mul_f32 v[232:233], v[116:117], v[120:121]
	v_pk_add_f32 v[218:219], v[236:237], v[218:219]
	v_pk_add_f32 v[220:221], v[236:237], v[220:221]
	v_pk_add_f32 v[226:227], v[236:237], v[226:227]
	v_pk_add_f32 v[228:229], v[236:237], v[228:229]
	v_rcp_f32_e32 v218, v218
	v_rcp_f32_e32 v219, v219
	v_rcp_f32_e32 v220, v220
	v_rcp_f32_e32 v221, v221
	v_rcp_f32_e32 v226, v226
	v_rcp_f32_e32 v227, v227
	v_rcp_f32_e32 v228, v228
	v_rcp_f32_e32 v229, v229
	v_pk_mul_f32 v[222:223], v[238:239], v[222:223]
	v_pk_mul_f32 v[224:225], v[238:239], v[224:225]
	v_pk_mul_f32 v[230:231], v[238:239], v[230:231]
	v_pk_mul_f32 v[232:233], v[238:239], v[232:233]
	v_pk_mul_f32 v[222:223], v[218:219], v[222:223]
	v_pk_mul_f32 v[224:225], v[220:221], v[224:225]
	v_pk_mul_f32 v[230:231], v[226:227], v[230:231]
	v_pk_mul_f32 v[232:233], v[228:229], v[232:233]
	v_med3_f32 v222, v222, s26, v209
	v_med3_f32 v223, v223, s26, v209
	v_med3_f32 v224, v224, s26, v209
	v_med3_f32 v225, v225, s26, v209
	v_med3_f32 v230, v230, s26, v209
	v_med3_f32 v231, v231, s26, v209
	v_med3_f32 v232, v232, s26, v209
	v_med3_f32 v233, v233, s26, v209
	v_cvt_pk_fp8_f32 v4, v222, v223
	v_cvt_pk_fp8_f32 v4, v224, v225 op_sel:[0,0,1]
	v_cvt_pk_fp8_f32 v5, v230, v231
	v_cvt_pk_fp8_f32 v5, v232, v233 op_sel:[0,0,1]
	v_lshl_add_u64 v[2:3], s[12:13], 0, v[130:131]
	s_mov_b32 s12, 0x8000
	v_add_co_u32_e32 v6, vcc, s12, v2
	s_nop 0
	v_addc_co_u32_e32 v7, vcc, 0, v3, vcc
	global_store_dwordx2 v[6:7], v[4:5], off
	v_pk_mul_f32 v[218:219], v[106:107], v[234:235]
	v_pk_mul_f32 v[220:221], v[108:109], v[234:235]
	v_pk_mul_f32 v[226:227], v[98:99], v[234:235]
	v_pk_mul_f32 v[228:229], v[100:101], v[234:235]
	v_exp_f32_e32 v218, v218
	v_exp_f32_e32 v219, v219
	v_exp_f32_e32 v220, v220
	v_exp_f32_e32 v221, v221
	v_exp_f32_e32 v226, v226
	v_exp_f32_e32 v227, v227
	v_exp_f32_e32 v228, v228
	v_exp_f32_e32 v229, v229
	v_pk_mul_f32 v[222:223], v[106:107], v[110:111]
	v_pk_mul_f32 v[224:225], v[108:109], v[112:113]
	v_pk_mul_f32 v[230:231], v[98:99], v[102:103]
	v_pk_mul_f32 v[232:233], v[100:101], v[104:105]
	v_pk_add_f32 v[218:219], v[236:237], v[218:219]
	v_pk_add_f32 v[220:221], v[236:237], v[220:221]
	v_pk_add_f32 v[226:227], v[236:237], v[226:227]
	v_pk_add_f32 v[228:229], v[236:237], v[228:229]
	v_rcp_f32_e32 v218, v218
	v_rcp_f32_e32 v219, v219
	v_rcp_f32_e32 v220, v220
	v_rcp_f32_e32 v221, v221
	v_rcp_f32_e32 v226, v226
	v_rcp_f32_e32 v227, v227
	v_rcp_f32_e32 v228, v228
	v_rcp_f32_e32 v229, v229
	v_pk_mul_f32 v[222:223], v[238:239], v[222:223]
	v_pk_mul_f32 v[224:225], v[238:239], v[224:225]
	v_pk_mul_f32 v[230:231], v[238:239], v[230:231]
	v_pk_mul_f32 v[232:233], v[238:239], v[232:233]
	v_pk_mul_f32 v[222:223], v[218:219], v[222:223]
	v_pk_mul_f32 v[224:225], v[220:221], v[224:225]
	v_pk_mul_f32 v[230:231], v[226:227], v[230:231]
	v_pk_mul_f32 v[232:233], v[228:229], v[232:233]
	v_med3_f32 v222, v222, s26, v209
	v_med3_f32 v223, v223, s26, v209
	v_med3_f32 v224, v224, s26, v209
	v_med3_f32 v225, v225, s26, v209
	v_med3_f32 v230, v230, s26, v209
	v_med3_f32 v231, v231, s26, v209
	v_med3_f32 v232, v232, s26, v209
	v_med3_f32 v233, v233, s26, v209
	v_cvt_pk_fp8_f32 v4, v222, v223
	v_cvt_pk_fp8_f32 v4, v224, v225 op_sel:[0,0,1]
	v_cvt_pk_fp8_f32 v5, v230, v231
	v_cvt_pk_fp8_f32 v5, v232, v233 op_sel:[0,0,1]
	s_mov_b32 s12, 0x10000
	v_add_co_u32_e32 v6, vcc, s12, v2
	s_nop 0
	v_addc_co_u32_e32 v7, vcc, 0, v3, vcc
	global_store_dwordx2 v[6:7], v[4:5], off
	v_pk_mul_f32 v[218:219], v[90:91], v[234:235]
	v_pk_mul_f32 v[220:221], v[92:93], v[234:235]
	v_pk_mul_f32 v[226:227], v[78:79], v[234:235]
	v_pk_mul_f32 v[228:229], v[80:81], v[234:235]
	v_exp_f32_e32 v218, v218
	v_exp_f32_e32 v219, v219
	v_exp_f32_e32 v220, v220
	v_exp_f32_e32 v221, v221
	v_exp_f32_e32 v226, v226
	v_exp_f32_e32 v227, v227
	v_exp_f32_e32 v228, v228
	v_exp_f32_e32 v229, v229
	v_pk_mul_f32 v[222:223], v[90:91], v[94:95]
	v_pk_mul_f32 v[224:225], v[92:93], v[96:97]
	v_pk_mul_f32 v[230:231], v[78:79], v[86:87]
	v_pk_mul_f32 v[232:233], v[80:81], v[88:89]
	v_pk_add_f32 v[218:219], v[236:237], v[218:219]
	v_pk_add_f32 v[220:221], v[236:237], v[220:221]
	v_pk_add_f32 v[226:227], v[236:237], v[226:227]
	v_pk_add_f32 v[228:229], v[236:237], v[228:229]
	v_rcp_f32_e32 v218, v218
	v_rcp_f32_e32 v219, v219
	v_rcp_f32_e32 v220, v220
	v_rcp_f32_e32 v221, v221
	v_rcp_f32_e32 v226, v226
	v_rcp_f32_e32 v227, v227
	v_rcp_f32_e32 v228, v228
	v_rcp_f32_e32 v229, v229
	v_pk_mul_f32 v[222:223], v[238:239], v[222:223]
	v_pk_mul_f32 v[224:225], v[238:239], v[224:225]
	v_pk_mul_f32 v[230:231], v[238:239], v[230:231]
	v_pk_mul_f32 v[232:233], v[238:239], v[232:233]
	v_pk_mul_f32 v[222:223], v[218:219], v[222:223]
	v_pk_mul_f32 v[224:225], v[220:221], v[224:225]
	v_pk_mul_f32 v[230:231], v[226:227], v[230:231]
	v_pk_mul_f32 v[232:233], v[228:229], v[232:233]
	v_med3_f32 v222, v222, s26, v209
	v_med3_f32 v223, v223, s26, v209
	v_med3_f32 v224, v224, s26, v209
	v_med3_f32 v225, v225, s26, v209
	v_med3_f32 v230, v230, s26, v209
	v_med3_f32 v231, v231, s26, v209
	v_med3_f32 v232, v232, s26, v209
	v_med3_f32 v233, v233, s26, v209
	v_cvt_pk_fp8_f32 v4, v222, v223
	v_cvt_pk_fp8_f32 v4, v224, v225 op_sel:[0,0,1]
	v_cvt_pk_fp8_f32 v5, v230, v231
	v_cvt_pk_fp8_f32 v5, v232, v233 op_sel:[0,0,1]
	s_mov_b32 s12, 0x18000
	v_add_co_u32_e32 v6, vcc, s12, v2
	s_nop 0
	v_addc_co_u32_e32 v7, vcc, 0, v3, vcc
	global_store_dwordx2 v[6:7], v[4:5], off
	v_pk_mul_f32 v[218:219], v[74:75], v[234:235]
	v_pk_mul_f32 v[220:221], v[76:77], v[234:235]
	v_pk_mul_f32 v[226:227], v[66:67], v[234:235]
	v_pk_mul_f32 v[228:229], v[68:69], v[234:235]
	v_exp_f32_e32 v218, v218
	v_exp_f32_e32 v219, v219
	v_exp_f32_e32 v220, v220
	v_exp_f32_e32 v221, v221
	v_exp_f32_e32 v226, v226
	v_exp_f32_e32 v227, v227
	v_exp_f32_e32 v228, v228
	v_exp_f32_e32 v229, v229
	v_pk_mul_f32 v[222:223], v[74:75], v[82:83]
	v_pk_mul_f32 v[224:225], v[76:77], v[84:85]
	v_pk_mul_f32 v[230:231], v[66:67], v[70:71]
	v_pk_mul_f32 v[232:233], v[68:69], v[72:73]
	v_pk_add_f32 v[218:219], v[236:237], v[218:219]
	v_pk_add_f32 v[220:221], v[236:237], v[220:221]
	v_pk_add_f32 v[226:227], v[236:237], v[226:227]
	v_pk_add_f32 v[228:229], v[236:237], v[228:229]
	v_rcp_f32_e32 v218, v218
	v_rcp_f32_e32 v219, v219
	v_rcp_f32_e32 v220, v220
	v_rcp_f32_e32 v221, v221
	v_rcp_f32_e32 v226, v226
	v_rcp_f32_e32 v227, v227
	v_rcp_f32_e32 v228, v228
	v_rcp_f32_e32 v229, v229
	v_pk_mul_f32 v[222:223], v[238:239], v[222:223]
	v_pk_mul_f32 v[224:225], v[238:239], v[224:225]
	v_pk_mul_f32 v[230:231], v[238:239], v[230:231]
	v_pk_mul_f32 v[232:233], v[238:239], v[232:233]
	v_pk_mul_f32 v[222:223], v[218:219], v[222:223]
	v_pk_mul_f32 v[224:225], v[220:221], v[224:225]
	v_pk_mul_f32 v[230:231], v[226:227], v[230:231]
	v_pk_mul_f32 v[232:233], v[228:229], v[232:233]
	v_med3_f32 v222, v222, s26, v209
	v_med3_f32 v223, v223, s26, v209
	v_med3_f32 v224, v224, s26, v209
	v_med3_f32 v225, v225, s26, v209
	v_med3_f32 v230, v230, s26, v209
	v_med3_f32 v231, v231, s26, v209
	v_med3_f32 v232, v232, s26, v209
	v_med3_f32 v233, v233, s26, v209
	v_cvt_pk_fp8_f32 v4, v222, v223
	v_cvt_pk_fp8_f32 v4, v224, v225 op_sel:[0,0,1]
	v_cvt_pk_fp8_f32 v5, v230, v231
	v_cvt_pk_fp8_f32 v5, v232, v233 op_sel:[0,0,1]
	s_mov_b32 s12, 0x40000
	v_add_co_u32_e32 v6, vcc, s12, v2
	s_nop 0
	v_addc_co_u32_e32 v7, vcc, 0, v3, vcc
	global_store_dwordx2 v[6:7], v[4:5], off
	v_pk_mul_f32 v[218:219], v[58:59], v[234:235]
	v_pk_mul_f32 v[220:221], v[60:61], v[234:235]
	v_pk_mul_f32 v[226:227], v[50:51], v[234:235]
	v_pk_mul_f32 v[228:229], v[52:53], v[234:235]
	v_exp_f32_e32 v218, v218
	v_exp_f32_e32 v219, v219
	v_exp_f32_e32 v220, v220
	v_exp_f32_e32 v221, v221
	v_exp_f32_e32 v226, v226
	v_exp_f32_e32 v227, v227
	v_exp_f32_e32 v228, v228
	v_exp_f32_e32 v229, v229
	v_pk_mul_f32 v[222:223], v[58:59], v[62:63]
	v_pk_mul_f32 v[224:225], v[60:61], v[64:65]
	v_pk_mul_f32 v[230:231], v[50:51], v[54:55]
	v_pk_mul_f32 v[232:233], v[52:53], v[56:57]
	v_pk_add_f32 v[218:219], v[236:237], v[218:219]
	v_pk_add_f32 v[220:221], v[236:237], v[220:221]
	v_pk_add_f32 v[226:227], v[236:237], v[226:227]
	v_pk_add_f32 v[228:229], v[236:237], v[228:229]
	v_rcp_f32_e32 v218, v218
	v_rcp_f32_e32 v219, v219
	v_rcp_f32_e32 v220, v220
	v_rcp_f32_e32 v221, v221
	v_rcp_f32_e32 v226, v226
	v_rcp_f32_e32 v227, v227
	v_rcp_f32_e32 v228, v228
	v_rcp_f32_e32 v229, v229
	v_pk_mul_f32 v[222:223], v[238:239], v[222:223]
	v_pk_mul_f32 v[224:225], v[238:239], v[224:225]
	v_pk_mul_f32 v[230:231], v[238:239], v[230:231]
	v_pk_mul_f32 v[232:233], v[238:239], v[232:233]
	v_pk_mul_f32 v[222:223], v[218:219], v[222:223]
	v_pk_mul_f32 v[224:225], v[220:221], v[224:225]
	v_pk_mul_f32 v[230:231], v[226:227], v[230:231]
	v_pk_mul_f32 v[232:233], v[228:229], v[232:233]
	v_med3_f32 v222, v222, s26, v209
	v_med3_f32 v223, v223, s26, v209
	v_med3_f32 v224, v224, s26, v209
	v_med3_f32 v225, v225, s26, v209
	v_med3_f32 v230, v230, s26, v209
	v_med3_f32 v231, v231, s26, v209
	v_med3_f32 v232, v232, s26, v209
	v_med3_f32 v233, v233, s26, v209
	v_cvt_pk_fp8_f32 v4, v222, v223
	v_cvt_pk_fp8_f32 v4, v224, v225 op_sel:[0,0,1]
	v_cvt_pk_fp8_f32 v5, v230, v231
	v_cvt_pk_fp8_f32 v5, v232, v233 op_sel:[0,0,1]
	s_mov_b32 s12, 0x48000
	v_add_co_u32_e32 v6, vcc, s12, v2
	s_nop 0
	v_addc_co_u32_e32 v7, vcc, 0, v3, vcc
	global_store_dwordx2 v[6:7], v[4:5], off
	v_pk_mul_f32 v[218:219], v[42:43], v[234:235]
	v_pk_mul_f32 v[220:221], v[44:45], v[234:235]
	v_pk_mul_f32 v[226:227], v[34:35], v[234:235]
	v_pk_mul_f32 v[228:229], v[36:37], v[234:235]
	v_exp_f32_e32 v218, v218
	v_exp_f32_e32 v219, v219
	v_exp_f32_e32 v220, v220
	v_exp_f32_e32 v221, v221
	v_exp_f32_e32 v226, v226
	v_exp_f32_e32 v227, v227
	v_exp_f32_e32 v228, v228
	v_exp_f32_e32 v229, v229
	v_pk_mul_f32 v[222:223], v[42:43], v[46:47]
	v_pk_mul_f32 v[224:225], v[44:45], v[48:49]
	v_pk_mul_f32 v[230:231], v[34:35], v[38:39]
	v_pk_mul_f32 v[232:233], v[36:37], v[40:41]
	v_pk_add_f32 v[218:219], v[236:237], v[218:219]
	v_pk_add_f32 v[220:221], v[236:237], v[220:221]
	v_pk_add_f32 v[226:227], v[236:237], v[226:227]
	v_pk_add_f32 v[228:229], v[236:237], v[228:229]
	v_rcp_f32_e32 v218, v218
	v_rcp_f32_e32 v219, v219
	v_rcp_f32_e32 v220, v220
	v_rcp_f32_e32 v221, v221
	v_rcp_f32_e32 v226, v226
	v_rcp_f32_e32 v227, v227
	v_rcp_f32_e32 v228, v228
	v_rcp_f32_e32 v229, v229
	v_pk_mul_f32 v[222:223], v[238:239], v[222:223]
	v_pk_mul_f32 v[224:225], v[238:239], v[224:225]
	v_pk_mul_f32 v[230:231], v[238:239], v[230:231]
	v_pk_mul_f32 v[232:233], v[238:239], v[232:233]
	v_pk_mul_f32 v[222:223], v[218:219], v[222:223]
	v_pk_mul_f32 v[224:225], v[220:221], v[224:225]
	v_pk_mul_f32 v[230:231], v[226:227], v[230:231]
	v_pk_mul_f32 v[232:233], v[228:229], v[232:233]
	v_med3_f32 v222, v222, s26, v209
	v_med3_f32 v223, v223, s26, v209
	v_med3_f32 v224, v224, s26, v209
	v_med3_f32 v225, v225, s26, v209
	v_med3_f32 v230, v230, s26, v209
	v_med3_f32 v231, v231, s26, v209
	v_med3_f32 v232, v232, s26, v209
	v_med3_f32 v233, v233, s26, v209
	v_cvt_pk_fp8_f32 v4, v222, v223
	v_cvt_pk_fp8_f32 v4, v224, v225 op_sel:[0,0,1]
	v_cvt_pk_fp8_f32 v5, v230, v231
	v_cvt_pk_fp8_f32 v5, v232, v233 op_sel:[0,0,1]
	s_mov_b32 s12, 0x50000
	v_add_co_u32_e32 v6, vcc, s12, v2
	s_nop 0
	v_addc_co_u32_e32 v7, vcc, 0, v3, vcc
	global_store_dwordx2 v[6:7], v[4:5], off
	v_pk_mul_f32 v[218:219], v[26:27], v[234:235]
	v_pk_mul_f32 v[220:221], v[28:29], v[234:235]
	v_pk_mul_f32 v[226:227], v[18:19], v[234:235]
	v_pk_mul_f32 v[228:229], v[20:21], v[234:235]
	v_exp_f32_e32 v218, v218
	v_exp_f32_e32 v219, v219
	v_exp_f32_e32 v220, v220
	v_exp_f32_e32 v221, v221
	v_exp_f32_e32 v226, v226
	v_exp_f32_e32 v227, v227
	v_exp_f32_e32 v228, v228
	v_exp_f32_e32 v229, v229
	v_pk_mul_f32 v[222:223], v[26:27], v[30:31]
	v_pk_mul_f32 v[224:225], v[28:29], v[32:33]
	v_pk_mul_f32 v[230:231], v[18:19], v[22:23]
	v_pk_mul_f32 v[232:233], v[20:21], v[24:25]
	v_pk_add_f32 v[218:219], v[236:237], v[218:219]
	v_pk_add_f32 v[220:221], v[236:237], v[220:221]
	v_pk_add_f32 v[226:227], v[236:237], v[226:227]
	v_pk_add_f32 v[228:229], v[236:237], v[228:229]
	v_rcp_f32_e32 v218, v218
	v_rcp_f32_e32 v219, v219
	v_rcp_f32_e32 v220, v220
	v_rcp_f32_e32 v221, v221
	v_rcp_f32_e32 v226, v226
	v_rcp_f32_e32 v227, v227
	v_rcp_f32_e32 v228, v228
	v_rcp_f32_e32 v229, v229
	v_pk_mul_f32 v[222:223], v[238:239], v[222:223]
	v_pk_mul_f32 v[224:225], v[238:239], v[224:225]
	v_pk_mul_f32 v[230:231], v[238:239], v[230:231]
	v_pk_mul_f32 v[232:233], v[238:239], v[232:233]
	v_pk_mul_f32 v[222:223], v[218:219], v[222:223]
	v_pk_mul_f32 v[224:225], v[220:221], v[224:225]
	v_pk_mul_f32 v[230:231], v[226:227], v[230:231]
	v_pk_mul_f32 v[232:233], v[228:229], v[232:233]
	v_med3_f32 v222, v222, s26, v209
	v_med3_f32 v223, v223, s26, v209
	v_med3_f32 v224, v224, s26, v209
	v_med3_f32 v225, v225, s26, v209
	v_med3_f32 v230, v230, s26, v209
	v_med3_f32 v231, v231, s26, v209
	v_med3_f32 v232, v232, s26, v209
	v_med3_f32 v233, v233, s26, v209
	v_cvt_pk_fp8_f32 v4, v222, v223
	v_cvt_pk_fp8_f32 v4, v224, v225 op_sel:[0,0,1]
	v_cvt_pk_fp8_f32 v5, v230, v231
	v_cvt_pk_fp8_f32 v5, v232, v233 op_sel:[0,0,1]
	v_add_co_u32_e32 v2, vcc, 0x58000, v2
	s_nop 0
	v_addc_co_u32_e32 v3, vcc, 0, v3, vcc
	s_and_b64 vcc, exec, s[4:5]
	s_mov_b32 s12, s6
	s_mov_b32 s59, s7
	s_mov_b64 s[60:61], s[8:9]
	s_mov_b64 s[18:19], s[10:11]
	global_store_dwordx2 v[2:3], v[4:5], off
	s_cbranch_vccz .LBB0_1416
	s_waitcnt vmcnt(0)
	s_cmpk_gt_u32 s27, 0xff
	s_movk_i32 s47, 0x900
	s_cbranch_scc1 .LBB0_1423
	s_barrier
